# P2 attention pipelined across units (next unit's K rows and q requested after this unit's QK^T; V rows land under QK^T+softmax); epilogue row-scale loads hoisted
# speedup vs baseline: 1.0086x; 1.0086x over previous
.LBB0_239:
	v_writelane_b32 v242, s80, 10
	s_cmp_lt_i32 s44, 3
	s_cselect_b64 s[0:1], -1, 0
	v_writelane_b32 v242, s81, 11
	v_writelane_b32 v242, s82, 12
	v_writelane_b32 v242, s83, 13
	v_writelane_b32 v242, s84, 14
	s_and_b64 s[0:1], s[0:1], s[4:5]
	v_writelane_b32 v242, s85, 15
	s_andn2_b64 vcc, exec, s[0:1]
	v_writelane_b32 v242, s86, 16
	v_writelane_b32 v242, s87, 17
	s_cbranch_vccnz .LBB0_246
	s_cmpk_gt_i32 s94, 0x11ff
	s_cbranch_scc1 .LBB0_246
	s_add_u32 s3, s46, 0x8e00000
	s_addc_u32 s33, s47, 0
	s_add_u32 s22, s46, 0x12e00000
	s_addc_u32 s23, s47, 0
	v_readlane_b32 s4, v242, 6
	s_add_u32 s24, s46, 0x100000
	v_lshrrev_b32_e32 v3, 4, v146
	s_mov_b32 s6, s4
	s_addc_u32 s25, s47, 0
	v_and_b32_e32 v5, 15, v0
	s_lshl_b32 s4, s4, 4
	s_waitcnt vmcnt(0)
	v_lshlrev_b32_e32 v6, 2, v3
	v_bfe_u32 v9, v0, 2, 2
	s_lshl_b32 s6, s6, 12
	v_lshlrev_b32_e32 v7, 3, v0
	v_sub_u32_e32 v8, v5, v6
	v_or3_b32 v9, s4, v9, v6
	v_lshrrev_b32_e32 v13, 3, v0
	s_add_i32 s6, s6, 0
	v_or_b32_e32 v58, s4, v5
	v_and_b32_e32 v2, 0x78, v7
	v_lshlrev_b32_e32 v4, 3, v3
	v_and_b32_e32 v7, 8, v7
	s_add_i32 s44, 0, 0x10000
	v_bitop3_b32 v13, v13, v5, 14 bitop3:0x6c
	v_bitop3_b32 v32, v3, v0, 15 bitop3:0x78
	v_lshl_add_u32 v33, v5, 8, s6
	v_bitop3_b32 v34, v3, v5, 4 bitop3:0x36
	v_bitop3_b32 v35, v3, v5, 8 bitop3:0x36
	v_bitop3_b32 v3, v3, v5, 12 bitop3:0x36
	v_cmp_gt_i32_e64 s[6:7], 1, v8
	v_cmp_gt_i32_e64 s[8:9], 2, v8
	v_cmp_gt_i32_e64 s[10:11], 3, v8
	v_cmp_gt_i32_e64 s[12:13], 4, v8
	v_cmp_lt_i32_e64 s[14:15], -1, v8
	v_cmp_lt_i32_e64 s[16:17], 0, v8
	v_cmp_lt_i32_e64 s[18:19], 1, v8
	v_cmp_lt_i32_e64 s[20:21], 2, v8
	v_lshlrev_b32_e32 v5, 8, v9
	v_lshlrev_b32_e32 v8, 1, v9
	v_and_b32_e32 v9, 14, v8
	v_add3_u32 v67, s44, v7, v5
	v_add3_u32 v68, s44, v5, v7
	v_bfe_u32 v5, v0, 1, 1
	v_or_b32_e32 v7, v9, v5
	v_lshlrev_b32_e32 v69, 4, v7
	v_or_b32_e32 v7, 2, v5
	v_bitop3_b32 v7, v8, v7, 14 bitop3:0x6c
	v_lshlrev_b32_e32 v70, 4, v7
	v_or_b32_e32 v7, 4, v5
	v_bitop3_b32 v7, v8, v7, 14 bitop3:0x6c
	v_or_b32_e32 v10, 0x200, v0
	s_cmpk_gt_u32 s96, 0x1ff
	v_lshlrev_b32_e32 v71, 4, v7
	v_or_b32_e32 v7, 6, v5
	v_lshrrev_b32_e32 v60, 4, v10
	v_or_b32_e32 v10, 0x600, v0
	s_cselect_b64 s[26:27], -1, 0
	s_cmpk_gt_u32 s96, 0x1bf
	v_bitop3_b32 v7, v8, v7, 14 bitop3:0x6c
	v_lshrrev_b32_e32 v62, 4, v10
	v_or_b32_e32 v10, 0xa00, v0
	s_cselect_b64 s[28:29], -1, 0
	s_cmpk_gt_u32 s96, 0x17f
	v_lshlrev_b32_e32 v72, 4, v7
	v_or_b32_e32 v7, 8, v5
	v_lshrrev_b32_e32 v64, 4, v10
	v_or_b32_e32 v10, 0xe00, v0
	s_cselect_b64 s[30:31], -1, 0
	s_cmpk_gt_u32 s96, 0x13f
	v_bitop3_b32 v7, v8, v7, 14 bitop3:0x6c
	v_lshrrev_b32_e32 v59, 4, v0
	v_lshrrev_b32_e32 v66, 4, v10
	s_cselect_b64 s[34:35], -1, 0
	s_cmpk_gt_u32 s96, 0xff
	v_lshlrev_b32_e32 v73, 4, v7
	v_or_b32_e32 v7, 10, v5
	v_or_b32_e32 v61, 64, v59
	v_or_b32_e32 v63, 0x80, v59
	v_or_b32_e32 v65, 0xc0, v59
	v_xor_b32_e32 v12, v59, v0
	v_xor_b32_e32 v16, v60, v0
	v_xor_b32_e32 v21, v62, v0
	v_xor_b32_e32 v26, v64, v0
	v_xor_b32_e32 v31, v66, v0
	s_cselect_b64 s[36:37], -1, 0
	s_cmpk_gt_u32 s96, 0xbf
	v_bitop3_b32 v7, v8, v7, 14 bitop3:0x6c
	v_lshlrev_b32_e32 v10, 8, v59
	v_lshlrev_b32_e32 v12, 4, v12
	v_lshlrev_b32_e32 v14, 8, v60
	v_lshlrev_b32_e32 v16, 4, v16
	v_lshlrev_b32_e32 v17, 8, v61
	v_lshlrev_b32_e32 v19, 8, v62
	v_lshlrev_b32_e32 v21, 4, v21
	v_lshlrev_b32_e32 v22, 8, v63
	v_lshlrev_b32_e32 v24, 8, v64
	v_lshlrev_b32_e32 v26, 4, v26
	v_lshlrev_b32_e32 v27, 8, v65
	v_lshlrev_b32_e32 v29, 8, v66
	v_lshlrev_b32_e32 v31, 4, v31
	s_cselect_b64 s[38:39], -1, 0
	s_cmpk_gt_u32 s96, 0x7f
	v_lshlrev_b32_e32 v74, 4, v7
	v_or_b32_e32 v7, 12, v5
	v_readlane_b32 s5, v242, 7
	v_add_u32_e32 v11, 0, v10
	v_and_b32_e32 v12, 0xf0, v12
	v_add_u32_e32 v10, s44, v10
	v_lshlrev_b32_e32 v13, 4, v13
	v_add_u32_e32 v15, 0, v14
	v_and_b32_e32 v16, 0xf0, v16
	v_add_u32_e32 v14, s44, v14
	v_add_u32_e32 v18, 0, v17
	v_add_u32_e32 v17, s44, v17
	v_add_u32_e32 v20, 0, v19
	v_and_b32_e32 v21, 0xf0, v21
	v_add_u32_e32 v19, s44, v19
	v_add_u32_e32 v23, 0, v22
	v_add_u32_e32 v22, s44, v22
	v_add_u32_e32 v25, 0, v24
	v_and_b32_e32 v26, 0xf0, v26
	v_add_u32_e32 v24, s44, v24
	v_add_u32_e32 v28, 0, v27
	v_add_u32_e32 v27, s44, v27
	v_add_u32_e32 v30, 0, v29
	v_and_b32_e32 v31, 0xf0, v31
	v_add_u32_e32 v29, s44, v29
	v_lshlrev_b32_e32 v32, 4, v32
	v_lshlrev_b32_e32 v34, 4, v34
	v_lshlrev_b32_e32 v35, 4, v35
	v_lshlrev_b32_e32 v3, 4, v3
	s_cselect_b64 s[40:41], -1, 0
	s_cmp_gt_u32 s96, 63
	v_bitop3_b32 v7, v8, v7, 14 bitop3:0x6c
	v_bitop3_b32 v5, v8, v5, 14 bitop3:0x4e
	v_lshlrev_b32_e32 v52, 1, v2
	v_mbcnt_lo_u32_b32 v2, -1, 0
	v_mov_b32_e32 v51, 0
	v_cmp_gt_u32_e64 s[4:5], 16, v146
	s_cselect_b64 s[42:43], -1, 0
	v_lshlrev_b32_e32 v75, 4, v7
	v_lshlrev_b32_e32 v76, 4, v5
	v_add_u32_e32 v77, 0x2000, v67
	v_add_u32_e32 v78, 0x4000, v67
	v_add_u32_e32 v79, 0x6000, v67
	s_movk_i32 s44, 0x1000
	v_add_u32_e32 v80, v11, v12
	v_add_u32_e32 v81, v10, v13
	v_add_u32_e32 v82, v15, v16
	v_add_u32_e32 v83, v14, v13
	v_add_u32_e32 v84, v18, v12
	v_add_u32_e32 v85, v17, v13
	v_add_u32_e32 v86, v20, v21
	v_add_u32_e32 v87, v19, v13
	v_add_u32_e32 v88, v23, v12
	v_add_u32_e32 v89, v22, v13
	v_add_u32_e32 v90, v25, v26
	v_add_u32_e32 v91, v24, v13
	v_add_u32_e32 v92, v28, v12
	v_add_u32_e32 v93, v27, v13
	v_add_u32_e32 v94, v30, v31
	v_add_u32_e32 v95, v29, v13
	v_add_u32_e32 v140, 0xc00, v12
	v_mov_b32_e32 v141, 0
	v_sub_u32_e32 v144, v13, v12
	v_add_u32_e32 v144, 0xc00, v144
	v_readlane_b32 s86, v242, 6
	s_nop 3
	s_lshl_b32 s86, s86, 10
	s_add_i32 s87, s86, 0x10000
	v_lshlrev_b32_e32 v54, 1, v4
	v_add_u32_e32 v96, v33, v32
	v_add_u32_e32 v97, v33, v34
	v_add_u32_e32 v98, v33, v35
	v_add_u32_e32 v99, v33, v3
	v_mbcnt_hi_u32_b32 v100, -1, v2
	s_mov_b32 s54, 0x3e0293ee
	s_movk_i32 s45, 0xc00
	v_lshlrev_b32_e32 v56, 1, v6
	v_mov_b32_e32 v101, 0xff800000
	v_mov_b32_e32 v102, 0x41b17218
	s_mov_b32 s55, s94
	s_mov_b32 s89, s94
	s_mul_i32 s90, s89, 0xaaab
	s_lshr_b32 s90, s90, 21
	s_mul_i32 s91, s90, 48
	s_sub_i32 s91, s89, s91
	s_lshr_b32 s92, s91, 4
	s_and_b32 s91, s91, 15
	s_mul_i32 s93, s90, 0x1556
	s_lshr_b32 s93, s93, 16
	s_mul_i32 s32, s93, 12
	s_sub_i32 s90, s90, s32
	s_lshr_b32 s32, s91, 2
	s_cmp_eq_u32 s92, 1
	s_cselect_b32 s32, s32, s91
	s_cmp_eq_u32 s92, 0
	s_cselect_b32 s32, 0, s32
	s_and_b32 s85, s91, 3
	s_cmp_eq_u32 s92, 1
	s_cselect_b32 s85, s85, 0
	s_cmp_eq_u32 s92, 0
	s_cselect_b32 s85, s91, s85
	s_lshl_b32 s93, s93, 11
	s_add_i32 s93, s93, s32
	s_mul_i32 s93, s93, 0x2800
	s_lshl_b32 s90, s90, 8
	s_add_i32 s93, s93, s90
	s_add_u32 s90, s3, s93
	s_addc_u32 s91, s33, 0
	s_mov_b32 s93, 0x28000
	s_movk_i32 s32, 0x7f
	s_cmp_eq_u32 s92, 1
	s_cselect_b32 s93, 0xa000, s93
	s_cselect_b32 s32, 0x1ff, s32
	s_cmp_eq_u32 s92, 0
	s_cselect_b32 s93, 0x2800, s93
	s_cselect_b32 s32, 0x7ff, s32
	s_lshl_b32 s85, s85, 7
	s_add_i32 s89, s85, 0xffffff80
	v_lshl_add_u64 v[192:193], s[90:91], 0, v[140:141]
	v_add_u32_e32 v194, s89, v59
	v_med3_i32 v194, v194, 0, s32
	v_mad_u64_u32 v[196:197], vcc, v194, s93, v[192:193]
	s_mov_b32 m0, s86
	s_nop 0
	global_load_lds_dwordx4 v[196:197], off
	v_add_u32_e32 v194, s89, v60
	v_med3_i32 v194, v194, 0, s32
	v_mad_u64_u32 v[198:199], vcc, v194, s93, v[192:193]
	s_add_i32 m0, s86, 8192
	s_nop 0
	global_load_lds_dwordx4 v[198:199], off
	v_add_u32_e32 v194, s89, v61
	v_med3_i32 v194, v194, 0, s32
	v_mad_u64_u32 v[200:201], vcc, v194, s93, v[192:193]
	s_add_i32 m0, s86, 16384
	s_nop 0
	global_load_lds_dwordx4 v[200:201], off
	v_add_u32_e32 v194, s89, v62
	v_med3_i32 v194, v194, 0, s32
	v_mad_u64_u32 v[202:203], vcc, v194, s93, v[192:193]
	s_add_i32 m0, s86, 24576
	s_nop 0
	global_load_lds_dwordx4 v[202:203], off
	v_add_u32_e32 v194, s89, v63
	v_med3_i32 v194, v194, 0, s32
	v_mad_u64_u32 v[204:205], vcc, v194, s93, v[192:193]
	s_add_i32 m0, s86, 32768
	s_nop 0
	global_load_lds_dwordx4 v[204:205], off
	v_add_u32_e32 v194, s89, v64
	v_med3_i32 v194, v194, 0, s32
	v_mad_u64_u32 v[206:207], vcc, v194, s93, v[192:193]
	s_add_i32 m0, s86, 40960
	s_nop 0
	global_load_lds_dwordx4 v[206:207], off
	v_add_u32_e32 v194, s89, v65
	v_med3_i32 v194, v194, 0, s32
	v_mad_u64_u32 v[208:209], vcc, v194, s93, v[192:193]
	s_add_i32 m0, s86, 49152
	s_nop 0
	global_load_lds_dwordx4 v[208:209], off
	v_add_u32_e32 v194, s89, v66
	v_med3_i32 v194, v194, 0, s32
	v_mad_u64_u32 v[210:211], vcc, v194, s93, v[192:193]
	s_add_i32 m0, s86, 57344
	s_nop 0
	global_load_lds_dwordx4 v[210:211], off
	v_mov_b32_e32 v132, s90
	v_mov_b32_e32 v133, s91
	v_add_co_u32_e32 v132, vcc, v132, v54
	s_nop 1
	v_addc_co_u32_e32 v133, vcc, 0, v133, vcc
	v_add_u32_e32 v194, s85, v58
	v_mad_u64_u32 v[132:133], vcc, v194, s93, v[132:133]
	global_load_dwordx4 v[212:215], v[132:133], off
	global_load_dwordx4 v[216:219], v[132:133], off offset:64
	global_load_dwordx4 v[220:223], v[132:133], off offset:128
	global_load_dwordx4 v[228:231], v[132:133], off offset:192
	s_branch .LBB0_243
.LBB0_242:
	s_or_b64 exec, exec, s[58:59]
	s_waitcnt lgkmcnt(0)
	s_nop 0
	s_add_i32 s55, s55, s88
	s_cmpk_lt_i32 s55, 0x1200
	s_cbranch_scc0 .LBB0_245
.LBB0_243:
	s_mul_hi_i32 s56, s55, 0x2aaaaaab
	s_lshr_b32 s57, s56, 31
	s_ashr_i32 s56, s56, 3
	s_mul_hi_i32 s60, s55, 0x38e38e39
	s_add_i32 s56, s56, s57
	s_lshr_b32 s61, s60, 31
	s_ashr_i32 s60, s60, 7
	s_mul_i32 s57, s56, 0xffffffd0
	s_add_i32 s64, s60, s61
	s_add_i32 s57, s55, s57
	s_mul_i32 s60, s64, -12
	s_ashr_i32 s58, s57, 4
	s_and_b32 s59, s55, 15
	s_add_i32 s56, s60, s56
	s_cmp_lt_u32 s57, 16
	s_cselect_b64 s[60:61], -1, 0
	s_cmp_eq_u32 s58, 1
	s_cselect_b64 s[62:63], -1, 0
	s_bfe_u32 s57, s55, 0x20002
	s_and_b64 s[66:67], s[62:63], exec
	s_cselect_b32 s57, s57, s59
	s_and_b64 s[66:67], s[60:61], exec
	s_cselect_b32 s57, 0, s57
	s_and_b32 s65, s55, 3
	s_and_b64 s[66:67], s[62:63], exec
	s_cselect_b32 s65, s65, 0
	s_and_b64 s[66:67], s[60:61], exec
	s_cselect_b32 s59, s59, s65
	s_ashr_i32 s65, s64, 31
	s_lshl_b64 s[64:65], s[64:65], 11
	s_or_b32 s66, s64, s57
	s_lshl_b32 s80, s59, 7
	s_mul_i32 s67, s66, 0x2800
	s_mul_hi_u32 s66, s66, 0x2800
	s_mul_i32 s68, s65, 0x2800
	s_add_i32 s82, s80, 0xffffff80
	s_add_i32 s66, s66, s68
	s_add_u32 s68, s3, s67
	s_addc_u32 s69, s33, s66
	s_lshl_b32 s66, s56, 7
	s_ashr_i32 s67, s66, 31
	s_lshl_b64 s[66:67], s[66:67], 1
	s_add_u32 s68, s68, s66
	s_addc_u32 s69, s69, s67
	s_and_b64 s[70:71], s[62:63], exec
	s_movk_i32 s70, 0x5000
	s_cselect_b32 s81, s70, 0x14000
	s_and_b64 s[70:71], s[60:61], exec
	s_cselect_b32 s83, 0x1400, s81
	v_add_u32_e32 v50, s80, v58
	v_mad_u64_u32 v[120:121], s[70:71], s83, v50, 0
	s_and_b64 s[70:71], s[62:63], exec
	s_movk_i32 s70, 0x7f
	s_cselect_b32 s80, 0x1ff, s70
	s_and_b64 s[70:71], s[60:61], exec
	s_cselect_b32 s84, 0x7ff, s80
	v_or_b32_e32 v2, s82, v59
	s_cmp_eq_u32 s59, 0
	v_or_b32_e32 v10, s82, v60
	s_cselect_b64 s[70:71], -1, 0
	v_min_i32_e32 v2, s84, v2
	v_min_i32_e32 v10, s84, v10
	v_mov_b32_e32 v53, v51
	v_cndmask_b32_e64 v2, v2, 0, s[70:71]
	v_cndmask_b32_e64 v10, v10, 0, s[70:71]
	v_lshl_add_u64 v[112:113], s[68:69], 0, v[140:141]
	v_mad_u64_u32 v[2:3], s[80:81], s83, v2, 0
	v_mad_u64_u32 v[10:11], s[80:81], s83, v10, 0
	v_lshl_add_u64 v[6:7], v[2:3], 1, v[112:113]
	v_lshl_add_u64 v[14:15], v[10:11], 1, v[112:113]
	v_or_b32_e32 v18, s82, v61
	s_nop 0
	s_nop 0
	v_add_co_u32_e32 v6, vcc, v144, v6
	v_min_i32_e32 v18, s84, v18
	v_add_u32_e32 v34, s82, v63
	v_addc_co_u32_e32 v7, vcc, 0, v7, vcc
	v_cndmask_b32_e64 v18, v18, 0, s[70:71]
	v_min_i32_e32 v34, s84, v34
	v_add_co_u32_e32 v14, vcc, v144, v14
	v_mad_u64_u32 v[18:19], s[70:71], s83, v18, 0
	v_mad_u64_u32 v[34:35], s[70:71], s83, v34, 0
	v_addc_co_u32_e32 v15, vcc, 0, v15, vcc
	v_lshl_add_u64 v[22:23], v[18:19], 1, v[112:113]
	v_lshl_add_u64 v[38:39], v[34:35], 1, v[112:113]
	s_nop 0
	s_nop 0
	v_add_co_u32_e32 v22, vcc, v144, v22
	v_or_b32_e32 v26, s82, v62
	s_nop 0
	v_addc_co_u32_e32 v23, vcc, 0, v23, vcc
	s_nop 0
	v_min_i32_e32 v27, s84, v26
	v_cmp_lt_i32_e32 vcc, -1, v26
	v_add_u32_e32 v42, s82, v64
	v_min_i32_e32 v42, s84, v42
	v_cndmask_b32_e32 v26, 0, v27, vcc
	s_nop 0
	v_mad_u64_u32 v[26:27], s[70:71], s83, v26, 0
	v_mad_u64_u32 v[42:43], s[70:71], s83, v42, 0
	v_lshl_add_u64 v[30:31], v[26:27], 1, v[112:113]
	v_lshl_add_u64 v[46:47], v[42:43], 1, v[112:113]
	s_nop 0
	v_add_u32_e32 v53, s82, v65
	s_nop 0
	s_nop 0
	v_add_co_u32_e32 v30, vcc, v144, v30
	v_min_i32_e32 v53, s84, v53
	s_nop 0
	v_addc_co_u32_e32 v31, vcc, 0, v31, vcc
	s_nop 0
	v_add_co_u32_e32 v38, vcc, v144, v38
	v_mad_u64_u32 v[104:105], s[70:71], s83, v53, 0
	v_add_u32_e32 v53, s82, v66
	v_addc_co_u32_e32 v39, vcc, 0, v39, vcc
	v_min_i32_e32 v53, s84, v53
	s_nop 0
	v_add_co_u32_e32 v46, vcc, v144, v46
	v_mad_u64_u32 v[114:115], s[70:71], s83, v53, 0
	s_nop 0
	v_addc_co_u32_e32 v47, vcc, 0, v47, vcc
	v_lshl_add_u64 v[108:109], v[104:105], 1, v[112:113]
	v_lshl_add_u64 v[116:117], v[114:115], 1, v[112:113]
	s_nop 0
	v_mov_b32_e32 v55, v51
	s_nop 0
	s_nop 0
	v_add_co_u32_e32 v108, vcc, v144, v108
	s_nop 0
	v_addc_co_u32_e32 v109, vcc, 0, v109, vcc
	s_nop 0
	v_add_co_u32_e32 v116, vcc, v144, v116
	s_nop 0
	v_addc_co_u32_e32 v117, vcc, 0, v117, vcc
	s_nop 0
	s_waitcnt vmcnt(0)
	s_waitcnt lgkmcnt(0)
	s_barrier
	s_mov_b32 m0, s87
	s_nop 0
	global_load_lds_dwordx4 v[6:7], off
	s_add_i32 m0, s87, 8192
	s_nop 0
	global_load_lds_dwordx4 v[14:15], off
	s_add_i32 m0, s87, 16384
	s_nop 0
	global_load_lds_dwordx4 v[22:23], off
	s_add_i32 m0, s87, 24576
	s_nop 0
	global_load_lds_dwordx4 v[30:31], off
	s_add_i32 m0, s87, 32768
	s_nop 0
	global_load_lds_dwordx4 v[38:39], off
	s_add_i32 m0, s87, 40960
	s_nop 0
	global_load_lds_dwordx4 v[46:47], off
	s_add_i32 m0, s87, 49152
	s_nop 0
	global_load_lds_dwordx4 v[108:109], off
	s_add_i32 m0, s87, 57344
	s_nop 0
	global_load_lds_dwordx4 v[116:117], off
	s_cmp_lg_u32 s59, 0
	s_mov_b32 s59, 0xff800000
	s_cselect_b64 s[68:69], -1, 0
	s_or_b64 s[70:71], s[68:69], s[26:27]
	s_and_b64 vcc, s[70:71], s[6:7]
	ds_read_b128 v[132:135], v96
	ds_read_b128 v[136:139], v97
	ds_read_b128 v[152:155], v98
	ds_read_b128 v[168:171], v99
	ds_read_b128 v[172:175], v96 offset:4096
	ds_read_b128 v[176:179], v97 offset:4096
	ds_read_b128 v[180:183], v98 offset:4096
	ds_read_b128 v[192:195], v99 offset:4096
	ds_read_b128 v[196:199], v96 offset:8192
	ds_read_b128 v[200:203], v97 offset:8192
	ds_read_b128 v[204:207], v98 offset:8192
	s_waitcnt lgkmcnt(10)
	v_mfma_f32_16x16x32_bf16 v[2:5], v[132:135], v[212:215], 0
	ds_read_b128 v[208:211], v99 offset:8192
	s_waitcnt lgkmcnt(10)
	v_mfma_f32_16x16x32_bf16 v[2:5], v[136:139], v[216:219], v[2:5]
	ds_read_b128 v[132:135], v96 offset:12288
	s_waitcnt lgkmcnt(10)
	v_mfma_f32_16x16x32_bf16 v[2:5], v[152:155], v[220:223], v[2:5]
	ds_read_b128 v[136:139], v97 offset:12288
	s_waitcnt lgkmcnt(10)
	v_mfma_f32_16x16x32_bf16 v[2:5], v[168:171], v[228:231], v[2:5]
	ds_read_b128 v[152:155], v98 offset:12288
	s_waitcnt lgkmcnt(10)
	v_mfma_f32_16x16x32_bf16 v[10:13], v[172:175], v[212:215], 0
	ds_read_b128 v[168:171], v99 offset:12288
	s_waitcnt lgkmcnt(10)
	v_mfma_f32_16x16x32_bf16 v[10:13], v[176:179], v[216:219], v[10:13]
	ds_read_b128 v[172:175], v96 offset:16384
	s_waitcnt lgkmcnt(10)
	v_mfma_f32_16x16x32_bf16 v[10:13], v[180:183], v[220:223], v[10:13]
	ds_read_b128 v[176:179], v97 offset:16384
	s_waitcnt lgkmcnt(10)
	v_mfma_f32_16x16x32_bf16 v[10:13], v[192:195], v[228:231], v[10:13]
	ds_read_b128 v[180:183], v98 offset:16384
	s_waitcnt lgkmcnt(10)
	v_mfma_f32_16x16x32_bf16 v[14:17], v[196:199], v[212:215], 0
	ds_read_b128 v[192:195], v99 offset:16384
	s_waitcnt lgkmcnt(10)
	v_mfma_f32_16x16x32_bf16 v[14:17], v[200:203], v[216:219], v[14:17]
	ds_read_b128 v[196:199], v96 offset:20480
	s_waitcnt lgkmcnt(10)
	v_mfma_f32_16x16x32_bf16 v[14:17], v[204:207], v[220:223], v[14:17]
	ds_read_b128 v[200:203], v97 offset:20480
	s_waitcnt lgkmcnt(10)
	v_mfma_f32_16x16x32_bf16 v[14:17], v[208:211], v[228:231], v[14:17]
	ds_read_b128 v[204:207], v98 offset:20480
	s_waitcnt lgkmcnt(10)
	v_mfma_f32_16x16x32_bf16 v[18:21], v[132:135], v[212:215], 0
	ds_read_b128 v[208:211], v99 offset:20480
	s_waitcnt lgkmcnt(10)
	v_mfma_f32_16x16x32_bf16 v[18:21], v[136:139], v[216:219], v[18:21]
	ds_read_b128 v[132:135], v96 offset:24576
	s_waitcnt lgkmcnt(10)
	v_mfma_f32_16x16x32_bf16 v[18:21], v[152:155], v[220:223], v[18:21]
	ds_read_b128 v[136:139], v97 offset:24576
	s_waitcnt lgkmcnt(10)
	v_mfma_f32_16x16x32_bf16 v[18:21], v[168:171], v[228:231], v[18:21]
	ds_read_b128 v[152:155], v98 offset:24576
	s_waitcnt lgkmcnt(10)
	v_mfma_f32_16x16x32_bf16 v[22:25], v[172:175], v[212:215], 0
	ds_read_b128 v[168:171], v99 offset:24576
	s_waitcnt lgkmcnt(10)
	v_mfma_f32_16x16x32_bf16 v[22:25], v[176:179], v[216:219], v[22:25]
	ds_read_b128 v[172:175], v96 offset:28672
	s_waitcnt lgkmcnt(10)
	v_mfma_f32_16x16x32_bf16 v[22:25], v[180:183], v[220:223], v[22:25]
	ds_read_b128 v[176:179], v97 offset:28672
	s_waitcnt lgkmcnt(10)
	v_mfma_f32_16x16x32_bf16 v[22:25], v[192:195], v[228:231], v[22:25]
	ds_read_b128 v[180:183], v98 offset:28672
	s_waitcnt lgkmcnt(10)
	v_mfma_f32_16x16x32_bf16 v[26:29], v[196:199], v[212:215], 0
	ds_read_b128 v[192:195], v99 offset:28672
	s_waitcnt lgkmcnt(10)
	v_mfma_f32_16x16x32_bf16 v[26:29], v[200:203], v[216:219], v[26:29]
	ds_read_b128 v[196:199], v96 offset:32768
	s_waitcnt lgkmcnt(10)
	v_mfma_f32_16x16x32_bf16 v[26:29], v[204:207], v[220:223], v[26:29]
	ds_read_b128 v[200:203], v97 offset:32768
	s_waitcnt lgkmcnt(10)
	v_mfma_f32_16x16x32_bf16 v[26:29], v[208:211], v[228:231], v[26:29]
	ds_read_b128 v[204:207], v98 offset:32768
	s_waitcnt lgkmcnt(10)
	v_mfma_f32_16x16x32_bf16 v[30:33], v[132:135], v[212:215], 0
	ds_read_b128 v[208:211], v99 offset:32768
	s_waitcnt lgkmcnt(10)
	v_mfma_f32_16x16x32_bf16 v[30:33], v[136:139], v[216:219], v[30:33]
	s_waitcnt lgkmcnt(9)
	v_mfma_f32_16x16x32_bf16 v[30:33], v[152:155], v[220:223], v[30:33]
	s_waitcnt lgkmcnt(8)
	v_mfma_f32_16x16x32_bf16 v[30:33], v[168:171], v[228:231], v[30:33]
	s_waitcnt lgkmcnt(7)
	v_mfma_f32_16x16x32_bf16 v[34:37], v[172:175], v[212:215], 0
	s_waitcnt lgkmcnt(6)
	v_mfma_f32_16x16x32_bf16 v[34:37], v[176:179], v[216:219], v[34:37]
	s_waitcnt lgkmcnt(5)
	v_mfma_f32_16x16x32_bf16 v[34:37], v[180:183], v[220:223], v[34:37]
	s_waitcnt lgkmcnt(4)
	v_mfma_f32_16x16x32_bf16 v[34:37], v[192:195], v[228:231], v[34:37]
	s_waitcnt lgkmcnt(3)
	v_mfma_f32_16x16x32_bf16 v[104:107], v[196:199], v[212:215], 0
	s_waitcnt lgkmcnt(2)
	v_mfma_f32_16x16x32_bf16 v[104:107], v[200:203], v[216:219], v[104:107]
	s_waitcnt lgkmcnt(1)
	v_mfma_f32_16x16x32_bf16 v[104:107], v[204:207], v[220:223], v[104:107]
	s_waitcnt lgkmcnt(0)
	v_mfma_f32_16x16x32_bf16 v[6:9], v[208:211], v[228:231], v[104:107]
	s_nop 2
	v_cndmask_b32_e32 v38, v101, v2, vcc
	s_and_b64 vcc, s[70:71], s[8:9]
	v_cndmask_b32_e32 v39, v101, v3, vcc
	s_and_b64 vcc, s[70:71], s[10:11]
	v_cndmask_b32_e32 v4, v101, v4, vcc
	s_and_b64 vcc, s[70:71], s[12:13]
	v_max3_f32 v2, v38, s59, v39
	v_cndmask_b32_e32 v5, v101, v5, vcc
	s_or_b64 vcc, s[28:29], s[68:69]
	v_max3_f32 v2, v2, v4, v5
	v_cndmask_b32_e32 v10, v101, v10, vcc
	v_cndmask_b32_e32 v11, v101, v11, vcc
	v_max3_f32 v2, v2, v10, v11
	v_cndmask_b32_e32 v12, v101, v12, vcc
	v_cndmask_b32_e32 v13, v101, v13, vcc
	s_or_b64 vcc, s[30:31], s[68:69]
	v_max3_f32 v2, v2, v12, v13
	v_cndmask_b32_e32 v14, v101, v14, vcc
	v_cndmask_b32_e32 v15, v101, v15, vcc
	v_max3_f32 v2, v2, v14, v15
	v_cndmask_b32_e32 v16, v101, v16, vcc
	v_cndmask_b32_e32 v17, v101, v17, vcc
	s_or_b64 vcc, s[34:35], s[68:69]
	v_max3_f32 v2, v2, v16, v17
	v_cndmask_b32_e32 v40, v101, v18, vcc
	v_cndmask_b32_e32 v41, v101, v19, vcc
	v_max3_f32 v2, v2, v40, v41
	v_cndmask_b32_e32 v20, v101, v20, vcc
	v_cndmask_b32_e32 v21, v101, v21, vcc
	s_or_b64 vcc, s[36:37], s[68:69]
	v_max3_f32 v2, v2, v20, v21
	v_cndmask_b32_e32 v22, v101, v22, vcc
	v_cndmask_b32_e32 v23, v101, v23, vcc
	v_max3_f32 v2, v2, v22, v23
	v_cndmask_b32_e32 v24, v101, v24, vcc
	v_cndmask_b32_e32 v42, v101, v25, vcc
	s_or_b64 vcc, s[38:39], s[68:69]
	v_max3_f32 v2, v2, v24, v42
	v_cndmask_b32_e32 v43, v101, v26, vcc
	v_cndmask_b32_e32 v44, v101, v27, vcc
	v_max3_f32 v2, v2, v43, v44
	v_cndmask_b32_e32 v45, v101, v28, vcc
	v_cndmask_b32_e32 v46, v101, v29, vcc
	s_or_b64 vcc, s[40:41], s[68:69]
	v_max3_f32 v2, v2, v45, v46
	v_cndmask_b32_e32 v47, v101, v30, vcc
	v_cndmask_b32_e32 v48, v101, v31, vcc
	v_max3_f32 v2, v2, v47, v48
	v_cndmask_b32_e32 v49, v101, v32, vcc
	v_cndmask_b32_e32 v53, v101, v33, vcc
	s_or_b64 vcc, s[42:43], s[68:69]
	v_max3_f32 v2, v2, v49, v53
	v_cndmask_b32_e32 v55, v101, v34, vcc
	v_cndmask_b32_e32 v57, v101, v35, vcc
	v_max3_f32 v2, v2, v55, v57
	v_cndmask_b32_e32 v103, v101, v36, vcc
	v_cndmask_b32_e32 v104, v101, v37, vcc
	v_max3_f32 v2, v2, v103, v104
	v_cndmask_b32_e64 v6, v101, v6, s[14:15]
	v_cndmask_b32_e64 v7, v101, v7, s[16:17]
	v_and_b32_e32 v18, 64, v100
	v_max3_f32 v3, v2, v6, v7
	v_cndmask_b32_e64 v2, v101, v9, s[20:21]
	v_xor_b32_e32 v9, 16, v100
	v_add_u32_e32 v18, 64, v18
	v_cmp_lt_i32_e32 vcc, v9, v18
	v_cndmask_b32_e64 v8, v101, v8, s[18:19]
	v_max3_f32 v3, v3, v8, v2
	v_cndmask_b32_e32 v9, v100, v9, vcc
	v_lshlrev_b32_e32 v105, 2, v9
	ds_bpermute_b32 v9, v105, v3
	s_and_b64 s[62:63], s[62:63], exec
	s_cselect_b32 s59, 2, 4
	s_and_b64 s[60:61], s[60:61], exec
	s_cselect_b32 s59, 0, s59
	s_waitcnt lgkmcnt(0)
	v_max_f32_e32 v9, v9, v9
	v_max_f32_e32 v3, v3, v9
	v_xor_b32_e32 v9, 32, v100
	v_cmp_lt_i32_e32 vcc, v9, v18
	s_nop 1
	v_cndmask_b32_e32 v9, v100, v9, vcc
	v_lshlrev_b32_e32 v106, 2, v9
	ds_bpermute_b32 v9, v106, v3
	s_waitcnt lgkmcnt(0)
	v_max_f32_e32 v9, v9, v9
	v_max_f32_e32 v3, v3, v9
	v_pk_mul_f32 v[18:19], v[2:3], s[54:55] op_sel_hi:[1,0]
	s_nop 0
	v_fma_f32 v4, v4, s54, -v19
	v_exp_f32_e32 v109, v4
	v_fma_f32 v4, v5, s54, -v19
	v_exp_f32_e32 v110, v4
	v_fma_f32 v4, v10, s54, -v19
	v_exp_f32_e32 v111, v4
	v_fma_f32 v4, v11, s54, -v19
	v_exp_f32_e32 v112, v4
	v_fma_f32 v4, v12, s54, -v19
	v_fma_f32 v2, v38, s54, -v19
	v_exp_f32_e32 v113, v4
	v_fma_f32 v4, v13, s54, -v19
	v_exp_f32_e32 v107, v2
	v_fma_f32 v9, v39, s54, -v19
	v_exp_f32_e32 v114, v4
	v_fma_f32 v4, v14, s54, -v19
	v_exp_f32_e32 v108, v9
	v_exp_f32_e32 v33, v4
	v_fma_f32 v4, v15, s54, -v19
	v_exp_f32_e32 v34, v4
	v_fma_f32 v4, v16, s54, -v19
	v_exp_f32_e32 v35, v4
	v_fma_f32 v4, v17, s54, -v19
	v_add_f32_e32 v2, 0, v107
	v_exp_f32_e32 v36, v4
	v_fma_f32 v4, v40, s54, -v19
	v_add_f32_e32 v2, v108, v2
	v_exp_f32_e32 v37, v4
	v_fma_f32 v4, v41, s54, -v19
	v_add_f32_e32 v2, v109, v2
	v_exp_f32_e32 v38, v4
	v_fma_f32 v4, v20, s54, -v19
	v_add_f32_e32 v2, v110, v2
	v_exp_f32_e32 v39, v4
	v_fma_f32 v4, v21, s54, -v19
	v_add_f32_e32 v2, v111, v2
	v_exp_f32_e32 v40, v4
	v_fma_f32 v4, v22, s54, -v19
	v_add_f32_e32 v2, v112, v2
	v_exp_f32_e32 v25, v4
	v_fma_f32 v4, v23, s54, -v19
	v_add_f32_e32 v2, v113, v2
	v_exp_f32_e32 v26, v4
	v_fma_f32 v4, v24, s54, -v19
	v_add_f32_e32 v2, v114, v2
	v_exp_f32_e32 v27, v4
	v_fma_f32 v4, v42, s54, -v19
	v_add_f32_e32 v2, v33, v2
	v_exp_f32_e32 v28, v4
	v_fma_f32 v4, v43, s54, -v19
	v_add_f32_e32 v2, v34, v2
	v_exp_f32_e32 v29, v4
	v_fma_f32 v4, v44, s54, -v19
	v_add_f32_e32 v2, v35, v2
	v_exp_f32_e32 v30, v4
	v_fma_f32 v4, v45, s54, -v19
	v_add_f32_e32 v2, v36, v2
	v_exp_f32_e32 v31, v4
	v_fma_f32 v4, v46, s54, -v19
	v_add_f32_e32 v2, v37, v2
	v_exp_f32_e32 v32, v4
	v_fma_f32 v4, v47, s54, -v19
	v_add_f32_e32 v2, v38, v2
	v_exp_f32_e32 v9, v4
	v_fma_f32 v4, v48, s54, -v19
	v_add_f32_e32 v2, v39, v2
	v_exp_f32_e32 v10, v4
	v_fma_f32 v4, v49, s54, -v19
	v_add_f32_e32 v2, v40, v2
	v_exp_f32_e32 v11, v4
	v_fma_f32 v4, v53, s54, -v19
	v_add_f32_e32 v2, v25, v2
	v_exp_f32_e32 v12, v4
	v_fma_f32 v4, v55, s54, -v19
	v_add_f32_e32 v2, v26, v2
	v_exp_f32_e32 v13, v4
	v_fma_f32 v4, v57, s54, -v19
	v_add_f32_e32 v2, v27, v2
	v_exp_f32_e32 v14, v4
	v_fma_f32 v4, v103, s54, -v19
	v_add_f32_e32 v2, v28, v2
	v_exp_f32_e32 v15, v4
	v_fma_f32 v4, v104, s54, -v19
	v_add_f32_e32 v2, v29, v2
	v_exp_f32_e32 v16, v4
	v_fma_f32 v4, v6, s54, -v19
	v_add_f32_e32 v2, v30, v2
	v_exp_f32_e32 v5, v4
	v_fma_f32 v4, v7, s54, -v19
	v_add_f32_e32 v2, v31, v2
	v_exp_f32_e32 v6, v4
	v_fma_f32 v4, v8, s54, -v19
	v_add_f32_e32 v2, v32, v2
	v_exp_f32_e32 v7, v4
	v_sub_f32_e32 v4, v18, v19
	v_add_u32_e32 v124, v67, v69
	v_add_u32_e32 v125, v67, v70
	v_add_u32_e32 v126, v67, v71
	v_add_u32_e32 v127, v67, v72
	v_add_u32_e32 v128, v67, v73
	v_add_u32_e32 v129, v67, v74
	v_add_u32_e32 v130, v67, v75
	v_add_u32_e32 v131, v67, v76
	s_waitcnt vmcnt(0)
	s_barrier
	s_add_i32 s89, s55, s88
	s_cmpk_lt_u32 s89, 0x1200
	s_cbranch_scc0 .Lp2_nopf
	s_mul_i32 s90, s89, 0xaaab
	s_lshr_b32 s90, s90, 21
	s_mul_i32 s91, s90, 48
	s_sub_i32 s91, s89, s91
	s_lshr_b32 s92, s91, 4
	s_and_b32 s91, s91, 15
	s_mul_i32 s93, s90, 0x1556
	s_lshr_b32 s93, s93, 16
	s_mul_i32 s32, s93, 12
	s_sub_i32 s90, s90, s32
	s_lshr_b32 s32, s91, 2
	s_cmp_eq_u32 s92, 1
	s_cselect_b32 s32, s32, s91
	s_cmp_eq_u32 s92, 0
	s_cselect_b32 s32, 0, s32
	s_and_b32 s85, s91, 3
	s_cmp_eq_u32 s92, 1
	s_cselect_b32 s85, s85, 0
	s_cmp_eq_u32 s92, 0
	s_cselect_b32 s85, s91, s85
	s_lshl_b32 s93, s93, 11
	s_add_i32 s93, s93, s32
	s_mul_i32 s93, s93, 0x2800
	s_lshl_b32 s90, s90, 8
	s_add_i32 s93, s93, s90
	s_add_u32 s90, s3, s93
	s_addc_u32 s91, s33, 0
	s_mov_b32 s93, 0x28000
	s_movk_i32 s32, 0x7f
	s_cmp_eq_u32 s92, 1
	s_cselect_b32 s93, 0xa000, s93
	s_cselect_b32 s32, 0x1ff, s32
	s_cmp_eq_u32 s92, 0
	s_cselect_b32 s93, 0x2800, s93
	s_cselect_b32 s32, 0x7ff, s32
	s_lshl_b32 s85, s85, 7
	s_add_i32 s89, s85, 0xffffff80
	v_lshl_add_u64 v[192:193], s[90:91], 0, v[140:141]
	v_add_u32_e32 v194, s89, v59
	v_med3_i32 v194, v194, 0, s32
	v_mad_u64_u32 v[196:197], vcc, v194, s93, v[192:193]
	s_mov_b32 m0, s86
	s_nop 0
	global_load_lds_dwordx4 v[196:197], off
	v_add_u32_e32 v194, s89, v60
	v_med3_i32 v194, v194, 0, s32
	v_mad_u64_u32 v[198:199], vcc, v194, s93, v[192:193]
	s_add_i32 m0, s86, 8192
	s_nop 0
	global_load_lds_dwordx4 v[198:199], off
	v_add_u32_e32 v194, s89, v61
	v_med3_i32 v194, v194, 0, s32
	v_mad_u64_u32 v[200:201], vcc, v194, s93, v[192:193]
	s_add_i32 m0, s86, 16384
	s_nop 0
	global_load_lds_dwordx4 v[200:201], off
	v_add_u32_e32 v194, s89, v62
	v_med3_i32 v194, v194, 0, s32
	v_mad_u64_u32 v[202:203], vcc, v194, s93, v[192:193]
	s_add_i32 m0, s86, 24576
	s_nop 0
	global_load_lds_dwordx4 v[202:203], off
	v_add_u32_e32 v194, s89, v63
	v_med3_i32 v194, v194, 0, s32
	v_mad_u64_u32 v[204:205], vcc, v194, s93, v[192:193]
	s_add_i32 m0, s86, 32768
	s_nop 0
	global_load_lds_dwordx4 v[204:205], off
	v_add_u32_e32 v194, s89, v64
	v_med3_i32 v194, v194, 0, s32
	v_mad_u64_u32 v[206:207], vcc, v194, s93, v[192:193]
	s_add_i32 m0, s86, 40960
	s_nop 0
	global_load_lds_dwordx4 v[206:207], off
	v_add_u32_e32 v194, s89, v65
	v_med3_i32 v194, v194, 0, s32
	v_mad_u64_u32 v[208:209], vcc, v194, s93, v[192:193]
	s_add_i32 m0, s86, 49152
	s_nop 0
	global_load_lds_dwordx4 v[208:209], off
	v_add_u32_e32 v194, s89, v66
	v_med3_i32 v194, v194, 0, s32
	v_mad_u64_u32 v[210:211], vcc, v194, s93, v[192:193]
	s_add_i32 m0, s86, 57344
	s_nop 0
	global_load_lds_dwordx4 v[210:211], off
	v_mov_b32_e32 v132, s90
	v_mov_b32_e32 v133, s91
	v_add_co_u32_e32 v132, vcc, v132, v54
	s_nop 1
	v_addc_co_u32_e32 v133, vcc, 0, v133, vcc
	v_add_u32_e32 v194, s85, v58
	v_mad_u64_u32 v[132:133], vcc, v194, s93, v[132:133]
	global_load_dwordx4 v[212:215], v[132:133], off
	global_load_dwordx4 v[216:219], v[132:133], off offset:64
	global_load_dwordx4 v[220:223], v[132:133], off offset:128
	global_load_dwordx4 v[228:231], v[132:133], off offset:192
.Lp2_nopf:
	ds_read_b64_tr_b16 v[196:197], v124
	ds_read_b64_tr_b16 v[198:199], v124 offset:4096
	ds_read_b64_tr_b16 v[200:201], v125
	ds_read_b64_tr_b16 v[202:203], v125 offset:4096
	ds_read_b64_tr_b16 v[204:205], v126
	ds_read_b64_tr_b16 v[206:207], v126 offset:4096
	v_cvt_pk_bf16_f32 v42, v107, v108
	v_cvt_pk_bf16_f32 v43, v109, v110
	v_cvt_pk_bf16_f32 v44, v111, v112
	v_cvt_pk_bf16_f32 v45, v113, v114
	v_add_f32_e32 v2, v9, v2
	v_add_f32_e32 v2, v10, v2
	v_add_f32_e32 v2, v11, v2
	v_add_f32_e32 v2, v12, v2
	v_add_f32_e32 v2, v13, v2
	v_add_f32_e32 v2, v14, v2
	v_add_f32_e32 v2, v15, v2
	v_add_f32_e32 v2, v16, v2
	v_exp_f32_e32 v8, v4
	v_add_f32_e32 v2, v5, v2
	v_add_f32_e32 v2, v6, v2
	v_add_f32_e32 v2, v7, v2
	v_cvt_pk_bf16_f32 v34, v33, v34
	v_cvt_pk_bf16_f32 v35, v35, v36
	v_cvt_pk_bf16_f32 v36, v37, v38
	v_cvt_pk_bf16_f32 v37, v39, v40
	v_add_f32_e32 v2, v8, v2
	ds_bpermute_b32 v4, v105, v2
	v_cvt_pk_bf16_f32 v26, v25, v26
	v_cvt_pk_bf16_f32 v27, v27, v28
	v_cvt_pk_bf16_f32 v28, v29, v30
	v_cvt_pk_bf16_f32 v29, v31, v32
	v_cvt_pk_bf16_f32 v10, v9, v10
	v_cvt_pk_bf16_f32 v11, v11, v12
	v_cvt_pk_bf16_f32 v12, v13, v14
	v_cvt_pk_bf16_f32 v13, v15, v16
	s_waitcnt lgkmcnt(0)
	v_add_f32_e32 v2, v2, v4
	ds_bpermute_b32 v4, v106, v2
	v_cvt_pk_bf16_f32 v6, v5, v6
	v_cvt_pk_bf16_f32 v7, v7, v8
	v_mov_b32_e32 v8, v51
	v_mov_b32_e32 v9, v51
	v_mov_b32_e32 v57, v51
	s_waitcnt lgkmcnt(0)
	v_add_f32_e32 v2, v2, v4
	v_div_scale_f32 v4, s[68:69], v2, v2, 1.0
	v_rcp_f32_e32 v5, v4
	v_mfma_f32_16x16x32_bf16 v[132:135], v[196:199], v[42:45], 0
	ds_read_b64_tr_b16 v[208:209], v127
	ds_read_b64_tr_b16 v[210:211], v127 offset:4096
	v_mfma_f32_16x16x32_bf16 v[136:139], v[200:203], v[42:45], 0
	ds_read_b64_tr_b16 v[196:197], v128
	ds_read_b64_tr_b16 v[198:199], v128 offset:4096
	v_mfma_f32_16x16x32_bf16 v[152:155], v[204:207], v[42:45], 0
	ds_read_b64_tr_b16 v[200:201], v129
	ds_read_b64_tr_b16 v[202:203], v129 offset:4096
	s_waitcnt lgkmcnt(4)
	v_mfma_f32_16x16x32_bf16 v[168:171], v[208:211], v[42:45], 0
	ds_read_b64_tr_b16 v[204:205], v130
	ds_read_b64_tr_b16 v[206:207], v130 offset:4096
	s_waitcnt lgkmcnt(4)
	v_mfma_f32_16x16x32_bf16 v[172:175], v[196:199], v[42:45], 0
	ds_read_b64_tr_b16 v[208:209], v131
	ds_read_b64_tr_b16 v[210:211], v131 offset:4096
	s_waitcnt lgkmcnt(4)
	v_mfma_f32_16x16x32_bf16 v[176:179], v[200:203], v[42:45], 0
	ds_read_b64_tr_b16 v[196:197], v124 offset:8192
	ds_read_b64_tr_b16 v[198:199], v124 offset:12288
	s_waitcnt lgkmcnt(4)
	v_mfma_f32_16x16x32_bf16 v[180:183], v[204:207], v[42:45], 0
	ds_read_b64_tr_b16 v[200:201], v125 offset:8192
	ds_read_b64_tr_b16 v[202:203], v125 offset:12288
	s_waitcnt lgkmcnt(4)
	v_mfma_f32_16x16x32_bf16 v[192:195], v[208:211], v[42:45], 0
	ds_read_b64_tr_b16 v[204:205], v126 offset:8192
	ds_read_b64_tr_b16 v[206:207], v126 offset:12288
	s_waitcnt lgkmcnt(4)
	v_mfma_f32_16x16x32_bf16 v[132:135], v[196:199], v[34:37], v[132:135]
	ds_read_b64_tr_b16 v[208:209], v127 offset:8192
	ds_read_b64_tr_b16 v[210:211], v127 offset:12288
	s_waitcnt lgkmcnt(4)
	v_mfma_f32_16x16x32_bf16 v[136:139], v[200:203], v[34:37], v[136:139]
	ds_read_b64_tr_b16 v[196:197], v128 offset:8192
	ds_read_b64_tr_b16 v[198:199], v128 offset:12288
	s_waitcnt lgkmcnt(4)
	v_mfma_f32_16x16x32_bf16 v[152:155], v[204:207], v[34:37], v[152:155]
	ds_read_b64_tr_b16 v[200:201], v129 offset:8192
	ds_read_b64_tr_b16 v[202:203], v129 offset:12288
	s_waitcnt lgkmcnt(4)
	v_mfma_f32_16x16x32_bf16 v[168:171], v[208:211], v[34:37], v[168:171]
	ds_read_b64_tr_b16 v[204:205], v130 offset:8192
	ds_read_b64_tr_b16 v[206:207], v130 offset:12288
	s_waitcnt lgkmcnt(4)
	v_mfma_f32_16x16x32_bf16 v[172:175], v[196:199], v[34:37], v[172:175]
	ds_read_b64_tr_b16 v[208:209], v131 offset:8192
	ds_read_b64_tr_b16 v[210:211], v131 offset:12288
	s_waitcnt lgkmcnt(4)
	v_mfma_f32_16x16x32_bf16 v[176:179], v[200:203], v[34:37], v[176:179]
	ds_read_b64_tr_b16 v[196:197], v124 offset:16384
	ds_read_b64_tr_b16 v[198:199], v124 offset:20480
	s_waitcnt lgkmcnt(4)
	v_mfma_f32_16x16x32_bf16 v[180:183], v[204:207], v[34:37], v[180:183]
	ds_read_b64_tr_b16 v[200:201], v125 offset:16384
	ds_read_b64_tr_b16 v[202:203], v125 offset:20480
	s_waitcnt lgkmcnt(4)
	v_mfma_f32_16x16x32_bf16 v[192:195], v[208:211], v[34:37], v[192:195]
	ds_read_b64_tr_b16 v[204:205], v126 offset:16384
	ds_read_b64_tr_b16 v[206:207], v126 offset:20480
	s_waitcnt lgkmcnt(4)
	v_mfma_f32_16x16x32_bf16 v[132:135], v[196:199], v[26:29], v[132:135]
	ds_read_b64_tr_b16 v[208:209], v127 offset:16384
	ds_read_b64_tr_b16 v[210:211], v127 offset:20480
	s_waitcnt lgkmcnt(4)
	v_mfma_f32_16x16x32_bf16 v[136:139], v[200:203], v[26:29], v[136:139]
	ds_read_b64_tr_b16 v[196:197], v128 offset:16384
	ds_read_b64_tr_b16 v[198:199], v128 offset:20480
	s_waitcnt lgkmcnt(4)
	v_mfma_f32_16x16x32_bf16 v[152:155], v[204:207], v[26:29], v[152:155]
	ds_read_b64_tr_b16 v[200:201], v129 offset:16384
	ds_read_b64_tr_b16 v[202:203], v129 offset:20480
	s_waitcnt lgkmcnt(4)
	v_mfma_f32_16x16x32_bf16 v[168:171], v[208:211], v[26:29], v[168:171]
	ds_read_b64_tr_b16 v[204:205], v130 offset:16384
	ds_read_b64_tr_b16 v[206:207], v130 offset:20480
	s_waitcnt lgkmcnt(4)
	v_mfma_f32_16x16x32_bf16 v[172:175], v[196:199], v[26:29], v[172:175]
	ds_read_b64_tr_b16 v[208:209], v131 offset:16384
	ds_read_b64_tr_b16 v[210:211], v131 offset:20480
	s_waitcnt lgkmcnt(4)
	v_mfma_f32_16x16x32_bf16 v[176:179], v[200:203], v[26:29], v[176:179]
	ds_read_b64_tr_b16 v[196:197], v124 offset:24576
	ds_read_b64_tr_b16 v[198:199], v124 offset:28672
	s_waitcnt lgkmcnt(4)
	v_mfma_f32_16x16x32_bf16 v[180:183], v[204:207], v[26:29], v[180:183]
	ds_read_b64_tr_b16 v[200:201], v125 offset:24576
	ds_read_b64_tr_b16 v[202:203], v125 offset:28672
	s_waitcnt lgkmcnt(4)
	v_mfma_f32_16x16x32_bf16 v[192:195], v[208:211], v[26:29], v[192:195]
	ds_read_b64_tr_b16 v[204:205], v126 offset:24576
	ds_read_b64_tr_b16 v[206:207], v126 offset:28672
	s_waitcnt lgkmcnt(4)
	v_mfma_f32_16x16x32_bf16 v[132:135], v[196:199], v[10:13], v[132:135]
	ds_read_b64_tr_b16 v[208:209], v127 offset:24576
	ds_read_b64_tr_b16 v[210:211], v127 offset:28672
	s_waitcnt lgkmcnt(4)
	v_mfma_f32_16x16x32_bf16 v[136:139], v[200:203], v[10:13], v[136:139]
	ds_read_b64_tr_b16 v[196:197], v128 offset:24576
	ds_read_b64_tr_b16 v[198:199], v128 offset:28672
	s_waitcnt lgkmcnt(4)
	v_mfma_f32_16x16x32_bf16 v[152:155], v[204:207], v[10:13], v[152:155]
	ds_read_b64_tr_b16 v[200:201], v129 offset:24576
	ds_read_b64_tr_b16 v[202:203], v129 offset:28672
	s_waitcnt lgkmcnt(4)
	v_mfma_f32_16x16x32_bf16 v[168:171], v[208:211], v[10:13], v[168:171]
	ds_read_b64_tr_b16 v[204:205], v130 offset:24576
	ds_read_b64_tr_b16 v[206:207], v130 offset:28672
	s_waitcnt lgkmcnt(4)
	v_mfma_f32_16x16x32_bf16 v[172:175], v[196:199], v[10:13], v[172:175]
	ds_read_b64_tr_b16 v[208:209], v131 offset:24576
	ds_read_b64_tr_b16 v[210:211], v131 offset:28672
	s_waitcnt lgkmcnt(4)
	v_mfma_f32_16x16x32_bf16 v[176:179], v[200:203], v[10:13], v[176:179]
	ds_read_b64_tr_b16 v[196:197], v124 offset:32768
	v_mov_b32_e32 v198, v51
	v_mov_b32_e32 v199, v51
	s_waitcnt lgkmcnt(3)
	v_mfma_f32_16x16x32_bf16 v[180:183], v[204:207], v[10:13], v[180:183]
	ds_read_b64_tr_b16 v[200:201], v125 offset:32768
	v_mov_b32_e32 v202, v51
	v_mov_b32_e32 v203, v51
	s_waitcnt lgkmcnt(2)
	v_mfma_f32_16x16x32_bf16 v[192:195], v[208:211], v[10:13], v[192:195]
	ds_read_b64_tr_b16 v[204:205], v126 offset:32768
	v_mov_b32_e32 v206, v51
	v_mov_b32_e32 v207, v51
	s_waitcnt lgkmcnt(2)
	v_mfma_f32_16x16x32_bf16 v[14:17], v[196:199], v[6:9], v[132:135]
	ds_read_b64_tr_b16 v[208:209], v127 offset:32768
	v_mov_b32_e32 v210, v51
	v_mov_b32_e32 v211, v51
	s_waitcnt lgkmcnt(2)
	v_mfma_f32_16x16x32_bf16 v[26:29], v[200:203], v[6:9], v[136:139]
	ds_read_b64_tr_b16 v[196:197], v128 offset:32768
	v_mov_b32_e32 v198, v51
	v_mov_b32_e32 v199, v51
	s_waitcnt lgkmcnt(2)
	v_mfma_f32_16x16x32_bf16 v[30:33], v[204:207], v[6:9], v[152:155]
	ds_read_b64_tr_b16 v[200:201], v129 offset:32768
	v_mov_b32_e32 v202, v51
	v_mov_b32_e32 v203, v51
	s_waitcnt lgkmcnt(2)
	v_mfma_f32_16x16x32_bf16 v[34:37], v[208:211], v[6:9], v[168:171]
	ds_read_b64_tr_b16 v[204:205], v130 offset:32768
	v_mov_b32_e32 v206, v51
	v_mov_b32_e32 v207, v51
	s_waitcnt lgkmcnt(2)
	v_mfma_f32_16x16x32_bf16 v[18:21], v[196:199], v[6:9], v[172:175]
	ds_read_b64_tr_b16 v[208:209], v131 offset:32768
	v_mov_b32_e32 v210, v51
	v_mov_b32_e32 v211, v51
	s_waitcnt lgkmcnt(2)
	v_mfma_f32_16x16x32_bf16 v[38:41], v[200:203], v[6:9], v[176:179]
	s_waitcnt lgkmcnt(1)
	v_mfma_f32_16x16x32_bf16 v[42:45], v[204:207], v[6:9], v[180:183]
	s_waitcnt lgkmcnt(0)
	v_mfma_f32_16x16x32_bf16 v[6:9], v[208:211], v[6:9], v[192:195]
	s_nop 2
	v_fma_f32 v10, -v4, v5, 1.0
	v_fmac_f32_e32 v5, v10, v5
	v_div_scale_f32 v10, vcc, 1.0, v2, 1.0
	v_mul_f32_e32 v11, v10, v5
	v_fma_f32 v12, -v4, v11, v10
	v_fmac_f32_e32 v11, v12, v5
	v_fma_f32 v4, -v4, v11, v10
	v_div_fmas_f32 v4, v4, v5, v11
	v_div_fixup_f32 v22, v4, v2, 1.0
	v_lshlrev_b64 v[4:5], s59, v[50:51]
	s_ashr_i32 s59, s58, 31
	s_lshl_b64 s[58:59], s[58:59], 14
	s_add_u32 s58, s58, s64
	s_addc_u32 s59, s59, s65
	s_or_b32 s58, s58, s57
	v_lshl_add_u64 v[4:5], s[58:59], 0, v[4:5]
	v_mov_b64_e32 v[10:11], s[22:23]
	v_mad_u64_u32 v[10:11], s[58:59], v4, s45, v[10:11]
	v_mad_i32_i24 v11, v5, s45, v11
	v_mul_f32_e32 v12, v22, v14
	v_mul_f32_e32 v13, v22, v15
	v_lshl_add_u64 v[10:11], v[10:11], 0, s[66:67]
	v_cvt_pk_bf16_f32 v12, v12, v13
	v_mul_f32_e32 v13, v22, v16
	v_lshl_add_u64 v[10:11], v[10:11], 0, v[56:57]
	v_mul_f32_e32 v14, v22, v17
	v_cvt_pk_bf16_f32 v13, v13, v14
	global_store_dwordx2 v[10:11], v[12:13], off
	v_mul_f32_e32 v12, v22, v26
	v_mul_f32_e32 v13, v22, v27
	v_cvt_pk_bf16_f32 v12, v12, v13
	v_mul_f32_e32 v13, v22, v28
	v_mul_f32_e32 v14, v22, v29
	v_cvt_pk_bf16_f32 v13, v13, v14
	global_store_dwordx2 v[10:11], v[12:13], off offset:32
	v_mul_f32_e32 v12, v22, v30
	v_mul_f32_e32 v13, v22, v31
	v_cvt_pk_bf16_f32 v12, v12, v13
	v_mul_f32_e32 v13, v22, v32
	v_mul_f32_e32 v14, v22, v33
	v_cvt_pk_bf16_f32 v13, v13, v14
	global_store_dwordx2 v[10:11], v[12:13], off offset:64
	v_mul_f32_e32 v12, v22, v34
	v_mul_f32_e32 v13, v22, v35
	v_cvt_pk_bf16_f32 v12, v12, v13
	v_mul_f32_e32 v13, v22, v36
	v_mul_f32_e32 v14, v22, v37
	v_cvt_pk_bf16_f32 v13, v13, v14
	global_store_dwordx2 v[10:11], v[12:13], off offset:96
	v_mul_f32_e32 v12, v22, v18
	v_mul_f32_e32 v13, v22, v19
	v_cvt_pk_bf16_f32 v12, v12, v13
	v_mul_f32_e32 v13, v22, v20
	v_mul_f32_e32 v14, v22, v21
	v_cvt_pk_bf16_f32 v13, v13, v14
	global_store_dwordx2 v[10:11], v[12:13], off offset:128
	v_mul_f32_e32 v12, v22, v38
	v_mul_f32_e32 v13, v22, v39
	v_cvt_pk_bf16_f32 v12, v12, v13
	v_mul_f32_e32 v13, v22, v40
	v_mul_f32_e32 v14, v22, v41
	v_cvt_pk_bf16_f32 v13, v13, v14
	global_store_dwordx2 v[10:11], v[12:13], off offset:160
	v_mul_f32_e32 v12, v22, v42
	v_mul_f32_e32 v13, v22, v43
	v_cvt_pk_bf16_f32 v12, v12, v13
	v_mul_f32_e32 v13, v22, v44
	v_mul_f32_e32 v6, v22, v6
	v_mul_f32_e32 v7, v22, v7
	v_mul_f32_e32 v14, v22, v45
	v_cvt_pk_bf16_f32 v13, v13, v14
	global_store_dwordx2 v[10:11], v[12:13], off offset:192
	v_cvt_pk_bf16_f32 v6, v6, v7
	v_mul_f32_e32 v7, v22, v8
	v_mul_f32_e32 v8, v22, v9
	v_cvt_pk_bf16_f32 v7, v7, v8
	global_store_dwordx2 v[10:11], v[6:7], off offset:224
	s_and_saveexec_b64 s[58:59], s[4:5]
	s_cbranch_execz .LBB0_242
	s_mov_b32 s57, 0x800000
	v_cmp_gt_f32_e32 vcc, s57, v2
	s_mov_b32 s57, 0x3f317217
	s_nop 0
	v_cndmask_b32_e64 v6, 0, 32, vcc
	v_ldexp_f32 v2, v2, v6
	v_log_f32_e32 v2, v2
	v_cndmask_b32_e32 v6, 0, v102, vcc
	v_mul_f32_e32 v7, 0x3f317217, v2
	v_fma_f32 v7, v2, s57, -v7
	v_fmac_f32_e32 v7, 0x3377d1cf, v2
	s_mov_b32 s57, 0x7f800000
	v_fmac_f32_e32 v7, 0x3f317217, v2
	v_cmp_lt_f32_e64 vcc, |v2|, s57
	s_ashr_i32 s57, s56, 31
	s_nop 0
	v_cndmask_b32_e32 v2, v2, v7, vcc
	v_sub_f32_e32 v6, v2, v6
	v_fmac_f32_e32 v6, 0x3db504f3, v3
	v_mad_u64_u32 v[2:3], s[60:61], v4, 48, s[24:25]
	v_mov_b32_e32 v4, v3
	v_mad_u64_u32 v[4:5], s[60:61], v5, 48, v[4:5]
	v_mov_b32_e32 v3, v4
	v_lshl_add_u64 v[2:3], s[56:57], 2, v[2:3]
	global_store_dword v[2:3], v6, off
	s_branch .LBB0_242
